# v58 plus NSA block top-k threshold search done bit-sliced (32x32 bit transpose per lane, one popcount per bit) instead of 31x32 compares
# speedup vs baseline: 1.0163x; 1.0163x over previous
; #define LAS __attribute__((address_space(3)))
; __device__ __forceinline__ float bf2f(unsigned v) { return __uint_as_float(v << 16); }
; __device__ __forceinline__ unsigned pk2(float lo, float hi) { const f32x2 f = {lo, hi}; const bf16n2 v = __builtin_convertvector(f, bf16n2); return __builtin_bit_cast(unsigned, v); }
; __device__ __forceinline__ float sigmoidf_(float x) { return __builtin_amdgcn_rcpf(1.0f + __expf(-x)); }
; __device__ __forceinline__ f32x4 unpack4(u32x2 z) { return (f32x4){__uint_as_float(z.x << 16), __uint_as_float(z.x & 0xffff0000u), __uint_as_float(z.y << 16), __uint_as_float(z.y & 0xffff0000u)}; }
;     ...
;             if (MODE != 0) scale *= sigmoidf_(bf2f(graw[qd]));
; #pragma unroll
;             for (int dt = 0; dt < 4; ++dt) { const f32x4 o = O[qd][dt] * scale; const int col = hh * 64 + 16 * dt + 4 * q;
;                 if (MODE == 0 || MODE == 1) { u32x2 w; w.x = pk2(o[0], o[1]); w.y = pk2(o[2], o[3]); *(u32x2*)(oout + (size_t)tq * 512 + col) = w; }
;                 else if (MODE == 2) { u32x2 w; w.x = pk2(o[0], o[1]); w.y = pk2(o[2], o[3]); *(u32x2*)((bf16_t*)nsaacc + (size_t)tq * 512 + col) = w; }
;                 else { const f32x4 t2 = (accp[dt] + unpack4(winp[dt])) + o; u32x2 w; w.x = pk2(t2[0], t2[1]); w.y = pk2(t2[2], t2[3]); *(u32x2*)(oout + (size_t)tq * 512 + col) = w; } }
;         }
;         if (MODE == 2 && DBG < 5) {
;             __syncthreads();
;             static_assert(TW == 8, "selection layout");
;             const int e = lane >> 3, sub = lane & 7, t = tw0 + e, cur = t >> 6;
;             const LAS float* sp = sscore + (wave * TW + e) * SSTR + 32 * sub;
;             unsigned key[32]; unsigned fmask = 0u;
; #pragma unroll
;             for (int i4 = 0; i4 < 8; ++i4) { const f32x4 v = *(const LAS f32x4*)(sp + 4 * i4);
; #pragma unroll
;                 for (int k = 0; k < 4; ++k) { const int i = 4 * i4 + k, j = 32 * sub + i; const bool forced = (j == 0 || j == cur || j == cur - 1);
;                     fmask |= forced ? (1u << i) : 0u; key[i] = (!forced && j < cur - 1) ? __float_as_uint(v[k]) + 1u : 0u; } }
.LBB0_920:
	s_waitcnt vmcnt(3)
	v_lshlrev_b32_e32 v54, 16, v149
	v_mul_f32_e32 v54, 0xbfb8aa3b, v54
	v_exp_f32_e32 v54, v54
	v_or_b32_e32 v55, s26, v140
	v_lshl_or_b32 v58, v55, 6, v141
	v_readlane_b32 s4, v252, 25
	v_add_f32_e32 v54, 1.0, v54
	v_rcp_f32_e32 v54, v54
	v_lshlrev_b64 v[56:57], 10, v[156:157]
	v_readlane_b32 s5, v252, 26
	v_ashrrev_i32_e32 v59, 31, v58
	v_pk_mul_f32 v[60:61], v[54:55], v[76:77] op_sel_hi:[0,1]
	v_lshl_add_u64 v[56:57], s[4:5], 0, v[56:57]
	s_waitcnt vmcnt(2)
	v_pk_mul_f32 v[66:67], v[54:55], v[74:75] op_sel_hi:[0,1]
	v_lshlrev_b64 v[58:59], 1, v[58:59]
	v_cvt_pk_bf16_f32 v66, v66, v67
	v_cvt_pk_bf16_f32 v67, v60, v61
	v_lshl_add_u64 v[56:57], v[56:57], 0, v[58:59]
	global_store_dwordx2 v[56:57], v[66:67], off
	v_pk_mul_f32 v[60:61], v[54:55], v[88:89] op_sel_hi:[0,1]
	v_pk_mul_f32 v[66:67], v[54:55], v[86:87] op_sel_hi:[0,1]
	v_cvt_pk_bf16_f32 v66, v66, v67
	v_cvt_pk_bf16_f32 v67, v60, v61
	global_store_dwordx2 v[56:57], v[66:67], off offset:32
	v_pk_mul_f32 v[60:61], v[54:55], v[84:85] op_sel_hi:[0,1]
	v_pk_mul_f32 v[66:67], v[54:55], v[82:83] op_sel_hi:[0,1]
	v_cvt_pk_bf16_f32 v66, v66, v67
	v_cvt_pk_bf16_f32 v67, v60, v61
	v_pk_mul_f32 v[60:61], v[54:55], v[72:73] op_sel_hi:[0,1]
	s_waitcnt vmcnt(2)
	v_lshlrev_b32_e32 v55, 16, v147
	v_mul_f32_e32 v55, 0xbfb8aa3b, v55
	global_store_dwordx2 v[56:57], v[66:67], off offset:64
	v_exp_f32_e32 v66, v55
	v_pk_mul_f32 v[54:55], v[54:55], v[70:71] op_sel_hi:[0,1]
	v_cvt_pk_bf16_f32 v54, v54, v55
	v_cvt_pk_bf16_f32 v55, v60, v61
	v_add_f32_e32 v60, 1.0, v66
	v_rcp_f32_e32 v60, v60
	global_store_dwordx2 v[56:57], v[54:55], off offset:96
	v_lshlrev_b64 v[54:55], 10, v[154:155]
	v_lshl_add_u64 v[54:55], s[4:5], 0, v[54:55]
	v_pk_mul_f32 v[56:57], v[60:61], v[64:65] op_sel_hi:[0,1]
	v_pk_mul_f32 v[62:63], v[60:61], v[62:63] op_sel_hi:[0,1]
	v_pk_mul_f32 v[52:53], v[60:61], v[52:53] op_sel_hi:[0,1]
	v_pk_mul_f32 v[50:51], v[60:61], v[50:51] op_sel_hi:[0,1]
	v_pk_mul_f32 v[48:49], v[60:61], v[48:49] op_sel_hi:[0,1]
	v_pk_mul_f32 v[46:47], v[60:61], v[46:47] op_sel_hi:[0,1]
	v_pk_mul_f32 v[44:45], v[60:61], v[44:45] op_sel_hi:[0,1]
	v_pk_mul_f32 v[42:43], v[60:61], v[42:43] op_sel_hi:[0,1]
	v_cvt_pk_bf16_f32 v62, v62, v63
	v_cvt_pk_bf16_f32 v63, v56, v57
	v_lshl_add_u64 v[54:55], v[54:55], 0, v[58:59]
	v_cvt_pk_bf16_f32 v50, v50, v51
	v_cvt_pk_bf16_f32 v51, v52, v53
	v_cvt_pk_bf16_f32 v46, v46, v47
	v_cvt_pk_bf16_f32 v47, v48, v49
	v_cvt_pk_bf16_f32 v42, v42, v43
	v_cvt_pk_bf16_f32 v43, v44, v45
	global_store_dwordx2 v[54:55], v[62:63], off
	global_store_dwordx2 v[54:55], v[50:51], off offset:32
	global_store_dwordx2 v[54:55], v[46:47], off offset:64
	global_store_dwordx2 v[54:55], v[42:43], off offset:96
	s_waitcnt lgkmcnt(0)
	s_barrier
	ds_read_b128 v[42:45], v170 offset:16384
	s_ashr_i32 s6, s11, 6
	v_readlane_b32 s4, v254, 43
	s_add_i32 s7, s6, -1
	v_cmp_ne_u32_e32 vcc, s6, v169
	v_readlane_b32 s5, v254, 44
	s_and_b64 s[4:5], s[4:5], vcc
	v_cmp_ne_u32_e32 vcc, s7, v169
	s_and_b64 s[26:27], s[4:5], vcc
	v_cmp_gt_i32_e32 vcc, s7, v169
	s_waitcnt lgkmcnt(0)
	v_add_u32_e32 v42, 1, v42
	s_and_b64 vcc, s[26:27], vcc
	v_cndmask_b32_e32 v42, 0, v42, vcc
	v_cmp_ne_u32_e32 vcc, s6, v171
	v_cmp_ne_u32_e64 s[14:15], s7, v171
	s_and_b64 s[36:37], vcc, s[14:15]
	v_cmp_gt_i32_e32 vcc, s7, v171
	v_add_u32_e32 v43, 1, v43
	s_and_b64 vcc, s[36:37], vcc
	v_cndmask_b32_e32 v43, 0, v43, vcc
	v_cmp_ne_u32_e32 vcc, s6, v172
	v_cmp_ne_u32_e64 s[14:15], s7, v172
	s_and_b64 s[38:39], vcc, s[14:15]
	v_cmp_gt_i32_e32 vcc, s7, v172
	v_add_u32_e32 v44, 1, v44
	s_and_b64 vcc, s[38:39], vcc
	v_cndmask_b32_e32 v44, 0, v44, vcc
	v_cmp_ne_u32_e32 vcc, s6, v173
	v_cmp_ne_u32_e64 s[14:15], s7, v173
	s_and_b64 s[46:47], vcc, s[14:15]
	v_cmp_gt_i32_e32 vcc, s7, v173
	ds_read_b128 v[46:49], v170 offset:16400
	ds_read_b128 v[50:53], v170 offset:16416
	ds_read_b128 v[54:57], v170 offset:16432
	v_add_u32_e32 v45, 1, v45
	s_and_b64 vcc, s[46:47], vcc
	v_cndmask_b32_e32 v45, 0, v45, vcc
	v_cmp_ne_u32_e32 vcc, s6, v174
	v_cmp_ne_u32_e64 s[14:15], s7, v174
	s_and_b64 s[48:49], vcc, s[14:15]
	v_cmp_gt_i32_e32 vcc, s7, v174
	s_waitcnt lgkmcnt(2)
	v_add_u32_e32 v46, 1, v46
	s_and_b64 vcc, s[48:49], vcc
	v_cndmask_b32_e32 v46, 0, v46, vcc
	v_cmp_ne_u32_e32 vcc, s6, v175
	v_cmp_ne_u32_e64 s[14:15], s7, v175
	s_and_b64 s[50:51], vcc, s[14:15]
	v_cmp_gt_i32_e32 vcc, s7, v175
	v_add_u32_e32 v47, 1, v47
	s_and_b64 vcc, s[50:51], vcc
	v_cndmask_b32_e32 v47, 0, v47, vcc
	v_cmp_ne_u32_e32 vcc, s6, v176
	v_cmp_ne_u32_e64 s[14:15], s7, v176
	s_and_b64 s[52:53], vcc, s[14:15]
	v_cmp_gt_i32_e32 vcc, s7, v176
	v_add_u32_e32 v48, 1, v48
	s_and_b64 vcc, s[52:53], vcc
	v_cndmask_b32_e32 v48, 0, v48, vcc
	v_cmp_ne_u32_e32 vcc, s6, v177
	v_cmp_ne_u32_e64 s[14:15], s7, v177
	s_and_b64 s[54:55], vcc, s[14:15]
	v_cmp_gt_i32_e32 vcc, s7, v177
	v_add_u32_e32 v49, 1, v49
	s_and_b64 vcc, s[54:55], vcc
	v_cndmask_b32_e32 v49, 0, v49, vcc
	v_cmp_ne_u32_e32 vcc, s6, v178
	v_cmp_ne_u32_e64 s[14:15], s7, v178
	s_and_b64 s[56:57], vcc, s[14:15]
	v_cmp_gt_i32_e32 vcc, s7, v178
	s_waitcnt lgkmcnt(1)
	v_add_u32_e32 v50, 1, v50
	s_and_b64 vcc, s[56:57], vcc
	v_cndmask_b32_e32 v50, 0, v50, vcc
	v_cmp_ne_u32_e32 vcc, s6, v179
	v_cmp_ne_u32_e64 s[14:15], s7, v179
	s_and_b64 s[58:59], vcc, s[14:15]
	v_cmp_gt_i32_e32 vcc, s7, v179
	v_add_u32_e32 v51, 1, v51
	s_and_b64 vcc, s[58:59], vcc
	v_cndmask_b32_e32 v51, 0, v51, vcc
	v_cmp_ne_u32_e32 vcc, s6, v180
	v_cmp_ne_u32_e64 s[14:15], s7, v180
	s_and_b64 s[60:61], vcc, s[14:15]
	v_cmp_gt_i32_e32 vcc, s7, v180
	v_add_u32_e32 v52, 1, v52
	s_and_b64 vcc, s[60:61], vcc
	v_cndmask_b32_e32 v52, 0, v52, vcc
	v_cmp_ne_u32_e32 vcc, s6, v181
	v_cmp_ne_u32_e64 s[14:15], s7, v181
	s_and_b64 s[62:63], vcc, s[14:15]
	v_cmp_gt_i32_e32 vcc, s7, v181
	v_add_u32_e32 v53, 1, v53
	s_and_b64 vcc, s[62:63], vcc
	v_cndmask_b32_e32 v53, 0, v53, vcc
	v_cmp_ne_u32_e32 vcc, s6, v182
	v_cmp_ne_u32_e64 s[14:15], s7, v182
	s_and_b64 s[64:65], vcc, s[14:15]
	v_cmp_gt_i32_e32 vcc, s7, v182
	s_waitcnt lgkmcnt(0)
; #define LAS __attribute__((address_space(3)))
; #define GRP8_SUM(x) do { x += __builtin_amdgcn_update_dpp(0, x, 0xB1, 0xf, 0xf, false); x += __builtin_amdgcn_update_dpp(0, x, 0x4E, 0xf, 0xf, false); x += __builtin_amdgcn_update_dpp(0, x, 0x141, 0xf, 0xf, false); } while (0)
;     ...
;             for (int i4 = 0; i4 < 8; ++i4) { const f32x4 v = *(const LAS f32x4*)(sp + 4 * i4);
; #pragma unroll
;                 for (int k = 0; k < 4; ++k) { const int i = 4 * i4 + k, j = 32 * sub + i; const bool forced = (j == 0 || j == cur || j == cur - 1);
;                     fmask |= forced ? (1u << i) : 0u; key[i] = (!forced && j < cur - 1) ? __float_as_uint(v[k]) + 1u : 0u; } }
;             const int K = 16 - (cur >= 2 ? 3 : cur + 1);
;     ...
;             unsigned Tk = 0u;
; #pragma unroll 1
;     ...
; #pragma unroll
;                 for (int i = 0; i < 32; ++i) cnt += (key[i] >= test) ? 1 : 0;
;                 GRP8_SUM(cnt);
;                 if (cnt >= K) Tk = test; }
	v_add_u32_e32 v54, 1, v54
	s_and_b64 vcc, s[64:65], vcc
	v_cndmask_b32_e32 v54, 0, v54, vcc
	v_cmp_ne_u32_e32 vcc, s6, v183
	v_cmp_ne_u32_e64 s[14:15], s7, v183
	s_and_b64 s[66:67], vcc, s[14:15]
	v_cmp_gt_i32_e32 vcc, s7, v183
	v_add_u32_e32 v55, 1, v55
	s_and_b64 vcc, s[66:67], vcc
	v_cndmask_b32_e32 v55, 0, v55, vcc
	v_cmp_ne_u32_e32 vcc, s6, v184
	v_cmp_ne_u32_e64 s[14:15], s7, v184
	s_and_b64 s[68:69], vcc, s[14:15]
	v_cmp_gt_i32_e32 vcc, s7, v184
	v_add_u32_e32 v56, 1, v56
	s_and_b64 vcc, s[68:69], vcc
	v_cndmask_b32_e32 v56, 0, v56, vcc
	v_cmp_ne_u32_e32 vcc, s6, v185
	v_cmp_ne_u32_e64 s[14:15], s7, v185
	ds_read_b128 v[58:61], v170 offset:16448
	ds_read_b128 v[62:65], v170 offset:16464
	s_and_b64 s[70:71], vcc, s[14:15]
	v_cmp_gt_i32_e32 vcc, s7, v185
	v_add_u32_e32 v57, 1, v57
	s_and_b64 vcc, s[70:71], vcc
	v_cndmask_b32_e32 v57, 0, v57, vcc
	v_cmp_ne_u32_e32 vcc, s6, v187
	v_cmp_ne_u32_e64 s[14:15], s7, v187
	s_and_b64 s[72:73], vcc, s[14:15]
	v_cmp_gt_i32_e32 vcc, s7, v187
	s_waitcnt lgkmcnt(1)
	v_add_u32_e32 v58, 1, v58
	s_and_b64 vcc, s[72:73], vcc
	v_cndmask_b32_e32 v58, 0, v58, vcc
	v_cmp_ne_u32_e32 vcc, s6, v189
	v_cmp_ne_u32_e64 s[14:15], s7, v189
	s_and_b64 s[74:75], vcc, s[14:15]
	v_cmp_gt_i32_e32 vcc, s7, v189
	v_add_u32_e32 v59, 1, v59
	s_and_b64 vcc, s[74:75], vcc
	v_cndmask_b32_e32 v59, 0, v59, vcc
	v_cmp_ne_u32_e32 vcc, s6, v195
	v_cmp_ne_u32_e64 s[14:15], s7, v195
	s_and_b64 s[76:77], vcc, s[14:15]
	v_cmp_gt_i32_e32 vcc, s7, v195
	v_add_u32_e32 v60, 1, v60
	s_and_b64 vcc, s[76:77], vcc
	v_cndmask_b32_e32 v60, 0, v60, vcc
	v_cmp_ne_u32_e32 vcc, s6, v196
	v_cmp_ne_u32_e64 s[14:15], s7, v196
	s_and_b64 s[78:79], vcc, s[14:15]
	v_cmp_gt_i32_e32 vcc, s7, v196
	v_add_u32_e32 v61, 1, v61
	s_and_b64 vcc, s[78:79], vcc
	v_cndmask_b32_e32 v61, 0, v61, vcc
	v_cmp_ne_u32_e32 vcc, s6, v197
	v_cmp_ne_u32_e64 s[14:15], s7, v197
	s_and_b64 s[80:81], vcc, s[14:15]
	v_cmp_gt_i32_e32 vcc, s7, v197
	s_waitcnt lgkmcnt(0)
	v_add_u32_e32 v62, 1, v62
	s_and_b64 vcc, s[80:81], vcc
	v_cndmask_b32_e32 v62, 0, v62, vcc
	v_cmp_ne_u32_e32 vcc, s6, v198
	v_cmp_ne_u32_e64 s[14:15], s7, v198
	s_and_b64 s[82:83], vcc, s[14:15]
	v_cmp_gt_i32_e32 vcc, s7, v198
	v_add_u32_e32 v63, 1, v63
	s_and_b64 vcc, s[82:83], vcc
	v_cndmask_b32_e32 v63, 0, v63, vcc
	v_cmp_ne_u32_e32 vcc, s6, v199
	v_cmp_ne_u32_e64 s[14:15], s7, v199
	s_and_b64 s[84:85], vcc, s[14:15]
	v_cmp_gt_i32_e32 vcc, s7, v199
	v_add_u32_e32 v64, 1, v64
	s_and_b64 vcc, s[84:85], vcc
	v_cndmask_b32_e32 v64, 0, v64, vcc
	v_cmp_ne_u32_e32 vcc, s6, v200
	v_cmp_ne_u32_e64 s[14:15], s7, v200
	ds_read_b128 v[66:69], v170 offset:16480
	ds_read_b128 v[70:73], v170 offset:16496
	s_and_b64 s[86:87], vcc, s[14:15]
	v_cmp_gt_i32_e32 vcc, s7, v200
	v_add_u32_e32 v65, 1, v65
	s_and_b64 vcc, s[86:87], vcc
	v_cndmask_b32_e32 v65, 0, v65, vcc
	v_cmp_ne_u32_e32 vcc, s6, v201
	v_cmp_ne_u32_e64 s[14:15], s7, v201
	s_and_b64 s[88:89], vcc, s[14:15]
	v_cmp_gt_i32_e32 vcc, s7, v201
	s_waitcnt lgkmcnt(1)
	v_add_u32_e32 v66, 1, v66
	s_and_b64 vcc, s[88:89], vcc
	v_cndmask_b32_e32 v66, 0, v66, vcc
	v_cmp_ne_u32_e32 vcc, s6, v202
	v_cmp_ne_u32_e64 s[14:15], s7, v202
	s_and_b64 s[90:91], vcc, s[14:15]
	v_cmp_gt_i32_e32 vcc, s7, v202
	v_add_u32_e32 v67, 1, v67
	s_and_b64 vcc, s[90:91], vcc
	v_cndmask_b32_e32 v67, 0, v67, vcc
	v_cmp_ne_u32_e32 vcc, s6, v203
	v_cmp_ne_u32_e64 s[14:15], s7, v203
	s_and_b64 s[94:95], vcc, s[14:15]
	v_cmp_gt_i32_e32 vcc, s7, v203
	v_add_u32_e32 v68, 1, v68
	s_and_b64 vcc, s[94:95], vcc
	v_cndmask_b32_e32 v68, 0, v68, vcc
	v_cmp_ne_u32_e32 vcc, s6, v204
	v_cmp_ne_u32_e64 s[14:15], s7, v204
	s_and_b64 s[28:29], vcc, s[14:15]
	v_cmp_gt_i32_e32 vcc, s7, v204
	v_add_u32_e32 v69, 1, v69
	s_and_b64 vcc, s[28:29], vcc
	v_cndmask_b32_e32 v69, 0, v69, vcc
	v_cmp_ne_u32_e32 vcc, s6, v205
	v_cmp_ne_u32_e64 s[14:15], s7, v205
	s_and_b64 s[92:93], vcc, s[14:15]
	v_cmp_gt_i32_e32 vcc, s7, v205
	s_waitcnt lgkmcnt(0)
	v_add_u32_e32 v70, 1, v70
	s_and_b64 vcc, s[92:93], vcc
	v_cndmask_b32_e32 v70, 0, v70, vcc
	v_cmp_ne_u32_e32 vcc, s6, v206
	v_cmp_ne_u32_e64 s[14:15], s7, v206
	s_and_b64 s[96:97], vcc, s[14:15]
	v_cmp_gt_i32_e32 vcc, s7, v206
	v_add_u32_e32 v71, 1, v71
	s_and_b64 vcc, s[96:97], vcc
	v_cndmask_b32_e32 v71, 0, v71, vcc
	v_cmp_ne_u32_e32 vcc, s6, v207
	v_cmp_ne_u32_e64 s[14:15], s7, v207
	s_and_b64 s[20:21], vcc, s[14:15]
	v_cmp_gt_i32_e32 vcc, s7, v207
	v_add_u32_e32 v72, 1, v72
	s_and_b64 vcc, s[20:21], vcc
	v_cndmask_b32_e32 v72, 0, v72, vcc
	v_cmp_ne_u32_e32 vcc, s6, v208
	v_cmp_ne_u32_e64 s[14:15], s7, v208
	s_and_b64 s[4:5], vcc, s[14:15]
	v_cmp_gt_i32_e32 vcc, s7, v208
	v_add_u32_e32 v73, 1, v73
	s_and_b64 vcc, s[4:5], vcc
	s_min_i32 s6, s6, 2
	v_cndmask_b32_e32 v73, 0, v73, vcc
	s_sub_i32 s6, 15, s6
	v_mov_b32_e32 v74, 0
	s_mov_b32 s7, 30
	s_mov_b32 s8, 0x5040100
	s_mov_b32 s9, 0x7060302
	v_perm_b32 v104, v58, v42, s8
	v_perm_b32 v105, v58, v42, s9
	v_perm_b32 v106, v59, v43, s8
	v_perm_b32 v107, v59, v43, s9
	v_perm_b32 v108, v60, v44, s8
	v_perm_b32 v109, v60, v44, s9
	v_perm_b32 v110, v61, v45, s8
	v_perm_b32 v111, v61, v45, s9
	v_perm_b32 v112, v62, v46, s8
	v_perm_b32 v113, v62, v46, s9
	v_perm_b32 v114, v63, v47, s8
	v_perm_b32 v115, v63, v47, s9
	v_perm_b32 v116, v64, v48, s8
	v_perm_b32 v117, v64, v48, s9
	v_perm_b32 v118, v65, v49, s8
	v_perm_b32 v119, v65, v49, s9
	v_perm_b32 v120, v66, v50, s8
	v_perm_b32 v121, v66, v50, s9
	v_perm_b32 v122, v67, v51, s8
	v_perm_b32 v123, v67, v51, s9
	v_perm_b32 v124, v68, v52, s8
	v_perm_b32 v125, v68, v52, s9
	v_perm_b32 v126, v69, v53, s8
	v_perm_b32 v127, v69, v53, s9
	v_perm_b32 v128, v70, v54, s8
	v_perm_b32 v129, v70, v54, s9
; #define GRP8_SUM(x) do { x += __builtin_amdgcn_update_dpp(0, x, 0xB1, 0xf, 0xf, false); x += __builtin_amdgcn_update_dpp(0, x, 0x4E, 0xf, 0xf, false); x += __builtin_amdgcn_update_dpp(0, x, 0x141, 0xf, 0xf, false); } while (0)
;     ...
;             unsigned Tk = 0u;
; #pragma unroll 1
;     ...
; #pragma unroll
;                 for (int i = 0; i < 32; ++i) cnt += (key[i] >= test) ? 1 : 0;
;                 GRP8_SUM(cnt);
;                 if (cnt >= K) Tk = test; }
	v_perm_b32 v130, v71, v55, s8
	v_perm_b32 v131, v71, v55, s9
	v_perm_b32 v132, v72, v56, s8
	v_perm_b32 v133, v72, v56, s9
	v_perm_b32 v134, v73, v57, s8
	v_perm_b32 v135, v73, v57, s9
	s_mov_b32 s8, 0x6020400
	s_mov_b32 s9, 0x7030501
	v_perm_b32 v136, v120, v104, s8
	v_perm_b32 v137, v120, v104, s9
	v_perm_b32 v42, v122, v106, s8
	v_perm_b32 v58, v122, v106, s9
	v_perm_b32 v43, v124, v108, s8
	v_perm_b32 v59, v124, v108, s9
	v_perm_b32 v44, v126, v110, s8
	v_perm_b32 v60, v126, v110, s9
	v_perm_b32 v45, v128, v112, s8
	v_perm_b32 v61, v128, v112, s9
	v_perm_b32 v46, v130, v114, s8
	v_perm_b32 v62, v130, v114, s9
	v_perm_b32 v47, v132, v116, s8
	v_perm_b32 v63, v132, v116, s9
	v_perm_b32 v48, v134, v118, s8
	v_perm_b32 v64, v134, v118, s9
	v_perm_b32 v49, v121, v105, s8
	v_perm_b32 v65, v121, v105, s9
	v_perm_b32 v50, v123, v107, s8
	v_perm_b32 v66, v123, v107, s9
	v_perm_b32 v51, v125, v109, s8
	v_perm_b32 v67, v125, v109, s9
	v_perm_b32 v52, v127, v111, s8
	v_perm_b32 v68, v127, v111, s9
	v_perm_b32 v53, v129, v113, s8
	v_perm_b32 v69, v129, v113, s9
	v_perm_b32 v54, v131, v115, s8
	v_perm_b32 v70, v131, v115, s9
	v_perm_b32 v55, v133, v117, s8
	v_perm_b32 v71, v133, v117, s9
	v_perm_b32 v56, v135, v119, s8
	v_perm_b32 v72, v135, v119, s9
	s_mov_b32 s7, 0xf0f0f0f
	s_mov_b32 s14, 0x33333333
	s_mov_b32 s15, 0x55555555
	v_lshlrev_b32_e32 v57, 4, v45
	v_lshrrev_b32_e32 v73, 4, v136
	v_bfi_b32 v136, s7, v136, v57
	v_bfi_b32 v45, s7, v73, v45
	v_lshlrev_b32_e32 v104, 4, v46
	v_lshrrev_b32_e32 v120, 4, v42
	v_bfi_b32 v42, s7, v42, v104
	v_bfi_b32 v46, s7, v120, v46
	v_lshlrev_b32_e32 v106, 4, v47
	v_lshrrev_b32_e32 v122, 4, v43
	v_bfi_b32 v43, s7, v43, v106
	v_bfi_b32 v47, s7, v122, v47
	v_lshlrev_b32_e32 v108, 4, v48
	v_lshrrev_b32_e32 v124, 4, v44
	v_bfi_b32 v44, s7, v44, v108
	v_bfi_b32 v48, s7, v124, v48
	v_lshlrev_b32_e32 v110, 4, v61
	v_lshrrev_b32_e32 v126, 4, v137
	v_bfi_b32 v137, s7, v137, v110
	v_bfi_b32 v61, s7, v126, v61
	v_lshlrev_b32_e32 v112, 4, v62
	v_lshrrev_b32_e32 v128, 4, v58
	v_bfi_b32 v58, s7, v58, v112
	v_bfi_b32 v62, s7, v128, v62
	v_lshlrev_b32_e32 v114, 4, v63
	v_lshrrev_b32_e32 v130, 4, v59
	v_bfi_b32 v59, s7, v59, v114
	v_bfi_b32 v63, s7, v130, v63
	v_lshlrev_b32_e32 v116, 4, v64
	v_lshrrev_b32_e32 v132, 4, v60
	v_bfi_b32 v60, s7, v60, v116
	v_bfi_b32 v64, s7, v132, v64
	v_lshlrev_b32_e32 v118, 4, v53
	v_lshrrev_b32_e32 v134, 4, v49
	v_bfi_b32 v49, s7, v49, v118
	v_bfi_b32 v53, s7, v134, v53
	v_lshlrev_b32_e32 v105, 4, v54
	v_lshrrev_b32_e32 v121, 4, v50
	v_bfi_b32 v50, s7, v50, v105
	v_bfi_b32 v54, s7, v121, v54
	v_lshlrev_b32_e32 v107, 4, v55
	v_lshrrev_b32_e32 v123, 4, v51
	v_bfi_b32 v51, s7, v51, v107
	v_bfi_b32 v55, s7, v123, v55
	v_lshlrev_b32_e32 v109, 4, v56
	v_lshrrev_b32_e32 v125, 4, v52
	v_bfi_b32 v52, s7, v52, v109
	v_bfi_b32 v56, s7, v125, v56
	v_lshlrev_b32_e32 v111, 4, v69
	v_lshrrev_b32_e32 v127, 4, v65
	v_bfi_b32 v65, s7, v65, v111
	v_bfi_b32 v69, s7, v127, v69
	v_lshlrev_b32_e32 v113, 4, v70
	v_lshrrev_b32_e32 v129, 4, v66
	v_bfi_b32 v66, s7, v66, v113
	v_bfi_b32 v70, s7, v129, v70
	v_lshlrev_b32_e32 v115, 4, v71
	v_lshrrev_b32_e32 v131, 4, v67
	v_bfi_b32 v67, s7, v67, v115
	v_bfi_b32 v71, s7, v131, v71
	v_lshlrev_b32_e32 v117, 4, v72
	v_lshrrev_b32_e32 v133, 4, v68
	v_bfi_b32 v68, s7, v68, v117
	v_bfi_b32 v72, s7, v133, v72
	v_lshlrev_b32_e32 v119, 2, v43
	v_lshrrev_b32_e32 v135, 2, v136
	v_bfi_b32 v136, s14, v136, v119
	v_bfi_b32 v43, s14, v135, v43
	v_lshlrev_b32_e32 v57, 2, v44
	v_lshrrev_b32_e32 v73, 2, v42
	v_bfi_b32 v42, s14, v42, v57
	v_bfi_b32 v44, s14, v73, v44
	v_lshlrev_b32_e32 v104, 2, v47
	v_lshrrev_b32_e32 v120, 2, v45
	v_bfi_b32 v45, s14, v45, v104
	v_bfi_b32 v47, s14, v120, v47
	v_lshlrev_b32_e32 v106, 2, v48
	v_lshrrev_b32_e32 v122, 2, v46
	v_bfi_b32 v46, s14, v46, v106
	v_bfi_b32 v48, s14, v122, v48
	v_lshlrev_b32_e32 v108, 2, v59
	v_lshrrev_b32_e32 v124, 2, v137
	v_bfi_b32 v137, s14, v137, v108
	v_bfi_b32 v59, s14, v124, v59
	v_lshlrev_b32_e32 v110, 2, v60
	v_lshrrev_b32_e32 v126, 2, v58
	v_bfi_b32 v58, s14, v58, v110
	v_bfi_b32 v60, s14, v126, v60
	v_lshlrev_b32_e32 v112, 2, v63
	v_lshrrev_b32_e32 v128, 2, v61
	v_bfi_b32 v61, s14, v61, v112
	v_bfi_b32 v63, s14, v128, v63
	v_lshlrev_b32_e32 v114, 2, v64
	v_lshrrev_b32_e32 v130, 2, v62
	v_bfi_b32 v62, s14, v62, v114
	v_bfi_b32 v64, s14, v130, v64
	v_lshlrev_b32_e32 v116, 2, v51
	v_lshrrev_b32_e32 v132, 2, v49
	v_bfi_b32 v49, s14, v49, v116
	v_bfi_b32 v51, s14, v132, v51
	v_lshlrev_b32_e32 v118, 2, v52
	v_lshrrev_b32_e32 v134, 2, v50
	v_bfi_b32 v50, s14, v50, v118
	v_bfi_b32 v52, s14, v134, v52
	v_lshlrev_b32_e32 v105, 2, v55
	v_lshrrev_b32_e32 v121, 2, v53
	v_bfi_b32 v53, s14, v53, v105
	v_bfi_b32 v55, s14, v121, v55
	v_lshlrev_b32_e32 v107, 2, v56
	v_lshrrev_b32_e32 v123, 2, v54
	v_bfi_b32 v54, s14, v54, v107
	v_bfi_b32 v56, s14, v123, v56
	v_lshlrev_b32_e32 v109, 2, v67
	v_lshrrev_b32_e32 v125, 2, v65
	v_bfi_b32 v65, s14, v65, v109
	v_bfi_b32 v67, s14, v125, v67
	v_lshlrev_b32_e32 v111, 2, v68
	v_lshrrev_b32_e32 v127, 2, v66
	v_bfi_b32 v66, s14, v66, v111
	v_bfi_b32 v68, s14, v127, v68
	v_lshlrev_b32_e32 v113, 2, v71
	v_lshrrev_b32_e32 v129, 2, v69
	v_bfi_b32 v69, s14, v69, v113
	v_bfi_b32 v71, s14, v129, v71
	v_lshlrev_b32_e32 v115, 2, v72
	v_lshrrev_b32_e32 v131, 2, v70
	v_bfi_b32 v70, s14, v70, v115
	v_bfi_b32 v72, s14, v131, v72
	v_lshlrev_b32_e32 v117, 1, v42
	v_lshrrev_b32_e32 v133, 1, v136
	v_bfi_b32 v136, s15, v136, v117
	v_bfi_b32 v42, s15, v133, v42
	v_lshlrev_b32_e32 v119, 1, v44
	v_lshrrev_b32_e32 v135, 1, v43
	v_bfi_b32 v43, s15, v43, v119
	v_bfi_b32 v44, s15, v135, v44
	v_lshlrev_b32_e32 v57, 1, v46
; #define GRP8_SUM(x) do { x += __builtin_amdgcn_update_dpp(0, x, 0xB1, 0xf, 0xf, false); x += __builtin_amdgcn_update_dpp(0, x, 0x4E, 0xf, 0xf, false); x += __builtin_amdgcn_update_dpp(0, x, 0x141, 0xf, 0xf, false); } while (0)
;     ...
;             unsigned Tk = 0u;
; #pragma unroll 1
;     ...
; #pragma unroll
;                 for (int i = 0; i < 32; ++i) cnt += (key[i] >= test) ? 1 : 0;
;                 GRP8_SUM(cnt);
;                 if (cnt >= K) Tk = test; }
	v_lshrrev_b32_e32 v73, 1, v45
	v_bfi_b32 v45, s15, v45, v57
	v_bfi_b32 v46, s15, v73, v46
	v_lshlrev_b32_e32 v104, 1, v48
	v_lshrrev_b32_e32 v120, 1, v47
	v_bfi_b32 v47, s15, v47, v104
	v_bfi_b32 v48, s15, v120, v48
	v_lshlrev_b32_e32 v106, 1, v58
	v_lshrrev_b32_e32 v122, 1, v137
	v_bfi_b32 v137, s15, v137, v106
	v_bfi_b32 v58, s15, v122, v58
	v_lshlrev_b32_e32 v108, 1, v60
	v_lshrrev_b32_e32 v124, 1, v59
	v_bfi_b32 v59, s15, v59, v108
	v_bfi_b32 v60, s15, v124, v60
	v_lshlrev_b32_e32 v110, 1, v62
	v_lshrrev_b32_e32 v126, 1, v61
	v_bfi_b32 v61, s15, v61, v110
	v_bfi_b32 v62, s15, v126, v62
	v_lshlrev_b32_e32 v112, 1, v64
	v_lshrrev_b32_e32 v128, 1, v63
	v_bfi_b32 v63, s15, v63, v112
	v_bfi_b32 v64, s15, v128, v64
	v_lshlrev_b32_e32 v114, 1, v50
	v_lshrrev_b32_e32 v130, 1, v49
	v_bfi_b32 v49, s15, v49, v114
	v_bfi_b32 v50, s15, v130, v50
	v_lshlrev_b32_e32 v116, 1, v52
	v_lshrrev_b32_e32 v132, 1, v51
	v_bfi_b32 v51, s15, v51, v116
	v_bfi_b32 v52, s15, v132, v52
	v_lshlrev_b32_e32 v118, 1, v54
	v_lshrrev_b32_e32 v134, 1, v53
	v_bfi_b32 v53, s15, v53, v118
	v_bfi_b32 v54, s15, v134, v54
	v_lshlrev_b32_e32 v105, 1, v56
	v_lshrrev_b32_e32 v121, 1, v55
	v_bfi_b32 v55, s15, v55, v105
	v_bfi_b32 v56, s15, v121, v56
	v_lshlrev_b32_e32 v107, 1, v66
	v_lshrrev_b32_e32 v123, 1, v65
	v_bfi_b32 v65, s15, v65, v107
	v_bfi_b32 v66, s15, v123, v66
	v_lshlrev_b32_e32 v109, 1, v68
	v_lshrrev_b32_e32 v125, 1, v67
	v_bfi_b32 v67, s15, v67, v109
	v_bfi_b32 v68, s15, v125, v68
	v_lshlrev_b32_e32 v111, 1, v70
	v_lshrrev_b32_e32 v127, 1, v69
	v_bfi_b32 v69, s15, v69, v111
	v_bfi_b32 v70, s15, v127, v70
	v_lshlrev_b32_e32 v113, 1, v72
	v_lshrrev_b32_e32 v129, 1, v71
	v_bfi_b32 v71, s15, v71, v113
	v_bfi_b32 v72, s15, v129, v72
	v_or3_b32 v115, v136, v42, v43
	v_or3_b32 v115, v115, v44, v45
	v_or3_b32 v115, v115, v46, v47
	v_or3_b32 v115, v115, v48, v137
	v_or3_b32 v115, v115, v58, v59
	v_or3_b32 v115, v115, v60, v61
	v_or3_b32 v115, v115, v62, v63
	v_or3_b32 v115, v115, v64, v49
	v_or3_b32 v115, v115, v50, v51
	v_or3_b32 v115, v115, v52, v53
	v_or3_b32 v115, v115, v54, v55
	v_or3_b32 v115, v115, v56, v65
	v_or3_b32 v115, v115, v66, v67
	v_or3_b32 v115, v115, v68, v69
	v_or3_b32 v115, v115, v70, v71
	v_or_b32_e32 v115, v115, v72
	v_not_b32_e32 v98, v72
	v_mov_b32_e32 v99, v72
	v_and_b32_e32 v100, v98, v71
	v_or_b32_e32 v101, v99, v100
	v_bcnt_u32_b32 v102, v101, 0
	s_nop 1
	v_add_u32_dpp v102, v102, v102 quad_perm:[1,0,3,2] row_mask:0xf bank_mask:0xf bound_ctrl:1
	s_nop 1
	v_add_u32_dpp v102, v102, v102 quad_perm:[2,3,0,1] row_mask:0xf bank_mask:0xf bound_ctrl:1
	s_nop 1
	v_add_u32_dpp v102, v102, v102 row_half_mirror row_mask:0xf bank_mask:0xf bound_ctrl:1
	v_cmp_le_i32_e32 vcc, s6, v102
	v_xor_b32_e32 v103, v98, v100
	s_nop 0
	v_cndmask_b32_e32 v98, v103, v100, vcc
	v_cndmask_b32_e32 v99, v101, v99, vcc
	v_and_b32_e32 v100, v98, v70
	v_or_b32_e32 v101, v99, v100
	v_bcnt_u32_b32 v102, v101, 0
	s_nop 1
	v_add_u32_dpp v102, v102, v102 quad_perm:[1,0,3,2] row_mask:0xf bank_mask:0xf bound_ctrl:1
	s_nop 1
	v_add_u32_dpp v102, v102, v102 quad_perm:[2,3,0,1] row_mask:0xf bank_mask:0xf bound_ctrl:1
	s_nop 1
	v_add_u32_dpp v102, v102, v102 row_half_mirror row_mask:0xf bank_mask:0xf bound_ctrl:1
	v_cmp_le_i32_e32 vcc, s6, v102
	v_xor_b32_e32 v103, v98, v100
	s_nop 0
	v_cndmask_b32_e32 v98, v103, v100, vcc
	v_cndmask_b32_e32 v99, v101, v99, vcc
	v_and_b32_e32 v100, v98, v69
	v_or_b32_e32 v101, v99, v100
	v_bcnt_u32_b32 v102, v101, 0
	s_nop 1
	v_add_u32_dpp v102, v102, v102 quad_perm:[1,0,3,2] row_mask:0xf bank_mask:0xf bound_ctrl:1
	s_nop 1
	v_add_u32_dpp v102, v102, v102 quad_perm:[2,3,0,1] row_mask:0xf bank_mask:0xf bound_ctrl:1
	s_nop 1
	v_add_u32_dpp v102, v102, v102 row_half_mirror row_mask:0xf bank_mask:0xf bound_ctrl:1
	v_cmp_le_i32_e32 vcc, s6, v102
	v_xor_b32_e32 v103, v98, v100
	s_nop 0
	v_cndmask_b32_e32 v98, v103, v100, vcc
	v_cndmask_b32_e32 v99, v101, v99, vcc
	v_and_b32_e32 v100, v98, v68
	v_or_b32_e32 v101, v99, v100
	v_bcnt_u32_b32 v102, v101, 0
	s_nop 1
	v_add_u32_dpp v102, v102, v102 quad_perm:[1,0,3,2] row_mask:0xf bank_mask:0xf bound_ctrl:1
	s_nop 1
	v_add_u32_dpp v102, v102, v102 quad_perm:[2,3,0,1] row_mask:0xf bank_mask:0xf bound_ctrl:1
	s_nop 1
	v_add_u32_dpp v102, v102, v102 row_half_mirror row_mask:0xf bank_mask:0xf bound_ctrl:1
	v_cmp_le_i32_e32 vcc, s6, v102
	v_xor_b32_e32 v103, v98, v100
	s_nop 0
	v_cndmask_b32_e32 v98, v103, v100, vcc
	v_cndmask_b32_e32 v99, v101, v99, vcc
	v_and_b32_e32 v100, v98, v67
	v_or_b32_e32 v101, v99, v100
	v_bcnt_u32_b32 v102, v101, 0
	s_nop 1
	v_add_u32_dpp v102, v102, v102 quad_perm:[1,0,3,2] row_mask:0xf bank_mask:0xf bound_ctrl:1
	s_nop 1
	v_add_u32_dpp v102, v102, v102 quad_perm:[2,3,0,1] row_mask:0xf bank_mask:0xf bound_ctrl:1
	s_nop 1
	v_add_u32_dpp v102, v102, v102 row_half_mirror row_mask:0xf bank_mask:0xf bound_ctrl:1
	v_cmp_le_i32_e32 vcc, s6, v102
	v_xor_b32_e32 v103, v98, v100
	s_nop 0
	v_cndmask_b32_e32 v98, v103, v100, vcc
	v_cndmask_b32_e32 v99, v101, v99, vcc
	v_and_b32_e32 v100, v98, v66
	v_or_b32_e32 v101, v99, v100
	v_bcnt_u32_b32 v102, v101, 0
	s_nop 1
	v_add_u32_dpp v102, v102, v102 quad_perm:[1,0,3,2] row_mask:0xf bank_mask:0xf bound_ctrl:1
	s_nop 1
	v_add_u32_dpp v102, v102, v102 quad_perm:[2,3,0,1] row_mask:0xf bank_mask:0xf bound_ctrl:1
	s_nop 1
	v_add_u32_dpp v102, v102, v102 row_half_mirror row_mask:0xf bank_mask:0xf bound_ctrl:1
	v_cmp_le_i32_e32 vcc, s6, v102
	v_xor_b32_e32 v103, v98, v100
	s_nop 0
	v_cndmask_b32_e32 v98, v103, v100, vcc
	v_cndmask_b32_e32 v99, v101, v99, vcc
	v_and_b32_e32 v100, v98, v65
	v_or_b32_e32 v101, v99, v100
	v_bcnt_u32_b32 v102, v101, 0
	s_nop 1
; #define GRP8_SUM(x) do { x += __builtin_amdgcn_update_dpp(0, x, 0xB1, 0xf, 0xf, false); x += __builtin_amdgcn_update_dpp(0, x, 0x4E, 0xf, 0xf, false); x += __builtin_amdgcn_update_dpp(0, x, 0x141, 0xf, 0xf, false); } while (0)
;     ...
;             unsigned Tk = 0u;
; #pragma unroll 1
;     ...
; #pragma unroll
;                 for (int i = 0; i < 32; ++i) cnt += (key[i] >= test) ? 1 : 0;
;                 GRP8_SUM(cnt);
;                 if (cnt >= K) Tk = test; }
	v_add_u32_dpp v102, v102, v102 quad_perm:[1,0,3,2] row_mask:0xf bank_mask:0xf bound_ctrl:1
	s_nop 1
	v_add_u32_dpp v102, v102, v102 quad_perm:[2,3,0,1] row_mask:0xf bank_mask:0xf bound_ctrl:1
	s_nop 1
	v_add_u32_dpp v102, v102, v102 row_half_mirror row_mask:0xf bank_mask:0xf bound_ctrl:1
	v_cmp_le_i32_e32 vcc, s6, v102
	v_xor_b32_e32 v103, v98, v100
	s_nop 0
	v_cndmask_b32_e32 v98, v103, v100, vcc
	v_cndmask_b32_e32 v99, v101, v99, vcc
	v_and_b32_e32 v100, v98, v56
	v_or_b32_e32 v101, v99, v100
	v_bcnt_u32_b32 v102, v101, 0
	s_nop 1
	v_add_u32_dpp v102, v102, v102 quad_perm:[1,0,3,2] row_mask:0xf bank_mask:0xf bound_ctrl:1
	s_nop 1
	v_add_u32_dpp v102, v102, v102 quad_perm:[2,3,0,1] row_mask:0xf bank_mask:0xf bound_ctrl:1
	s_nop 1
	v_add_u32_dpp v102, v102, v102 row_half_mirror row_mask:0xf bank_mask:0xf bound_ctrl:1
	v_cmp_le_i32_e32 vcc, s6, v102
	v_xor_b32_e32 v103, v98, v100
	s_nop 0
	v_cndmask_b32_e32 v98, v103, v100, vcc
	v_cndmask_b32_e32 v99, v101, v99, vcc
	v_and_b32_e32 v100, v98, v55
	v_or_b32_e32 v101, v99, v100
	v_bcnt_u32_b32 v102, v101, 0
	s_nop 1
	v_add_u32_dpp v102, v102, v102 quad_perm:[1,0,3,2] row_mask:0xf bank_mask:0xf bound_ctrl:1
	s_nop 1
	v_add_u32_dpp v102, v102, v102 quad_perm:[2,3,0,1] row_mask:0xf bank_mask:0xf bound_ctrl:1
	s_nop 1
	v_add_u32_dpp v102, v102, v102 row_half_mirror row_mask:0xf bank_mask:0xf bound_ctrl:1
	v_cmp_le_i32_e32 vcc, s6, v102
	v_xor_b32_e32 v103, v98, v100
	s_nop 0
	v_cndmask_b32_e32 v98, v103, v100, vcc
	v_cndmask_b32_e32 v99, v101, v99, vcc
	v_and_b32_e32 v100, v98, v54
	v_or_b32_e32 v101, v99, v100
	v_bcnt_u32_b32 v102, v101, 0
	s_nop 1
	v_add_u32_dpp v102, v102, v102 quad_perm:[1,0,3,2] row_mask:0xf bank_mask:0xf bound_ctrl:1
	s_nop 1
	v_add_u32_dpp v102, v102, v102 quad_perm:[2,3,0,1] row_mask:0xf bank_mask:0xf bound_ctrl:1
	s_nop 1
	v_add_u32_dpp v102, v102, v102 row_half_mirror row_mask:0xf bank_mask:0xf bound_ctrl:1
	v_cmp_le_i32_e32 vcc, s6, v102
	v_xor_b32_e32 v103, v98, v100
	s_nop 0
	v_cndmask_b32_e32 v98, v103, v100, vcc
	v_cndmask_b32_e32 v99, v101, v99, vcc
	v_and_b32_e32 v100, v98, v53
	v_or_b32_e32 v101, v99, v100
	v_bcnt_u32_b32 v102, v101, 0
	s_nop 1
	v_add_u32_dpp v102, v102, v102 quad_perm:[1,0,3,2] row_mask:0xf bank_mask:0xf bound_ctrl:1
	s_nop 1
	v_add_u32_dpp v102, v102, v102 quad_perm:[2,3,0,1] row_mask:0xf bank_mask:0xf bound_ctrl:1
	s_nop 1
	v_add_u32_dpp v102, v102, v102 row_half_mirror row_mask:0xf bank_mask:0xf bound_ctrl:1
	v_cmp_le_i32_e32 vcc, s6, v102
	v_xor_b32_e32 v103, v98, v100
	s_nop 0
	v_cndmask_b32_e32 v98, v103, v100, vcc
	v_cndmask_b32_e32 v99, v101, v99, vcc
	v_and_b32_e32 v100, v98, v52
	v_or_b32_e32 v101, v99, v100
	v_bcnt_u32_b32 v102, v101, 0
	s_nop 1
	v_add_u32_dpp v102, v102, v102 quad_perm:[1,0,3,2] row_mask:0xf bank_mask:0xf bound_ctrl:1
	s_nop 1
	v_add_u32_dpp v102, v102, v102 quad_perm:[2,3,0,1] row_mask:0xf bank_mask:0xf bound_ctrl:1
	s_nop 1
	v_add_u32_dpp v102, v102, v102 row_half_mirror row_mask:0xf bank_mask:0xf bound_ctrl:1
	v_cmp_le_i32_e32 vcc, s6, v102
	v_xor_b32_e32 v103, v98, v100
	s_nop 0
	v_cndmask_b32_e32 v98, v103, v100, vcc
	v_cndmask_b32_e32 v99, v101, v99, vcc
	v_and_b32_e32 v100, v98, v51
	v_or_b32_e32 v101, v99, v100
	v_bcnt_u32_b32 v102, v101, 0
	s_nop 1
	v_add_u32_dpp v102, v102, v102 quad_perm:[1,0,3,2] row_mask:0xf bank_mask:0xf bound_ctrl:1
	s_nop 1
	v_add_u32_dpp v102, v102, v102 quad_perm:[2,3,0,1] row_mask:0xf bank_mask:0xf bound_ctrl:1
	s_nop 1
	v_add_u32_dpp v102, v102, v102 row_half_mirror row_mask:0xf bank_mask:0xf bound_ctrl:1
	v_cmp_le_i32_e32 vcc, s6, v102
	v_xor_b32_e32 v103, v98, v100
	s_nop 0
	v_cndmask_b32_e32 v98, v103, v100, vcc
	v_cndmask_b32_e32 v99, v101, v99, vcc
	v_and_b32_e32 v100, v98, v50
	v_or_b32_e32 v101, v99, v100
	v_bcnt_u32_b32 v102, v101, 0
	s_nop 1
	v_add_u32_dpp v102, v102, v102 quad_perm:[1,0,3,2] row_mask:0xf bank_mask:0xf bound_ctrl:1
	s_nop 1
	v_add_u32_dpp v102, v102, v102 quad_perm:[2,3,0,1] row_mask:0xf bank_mask:0xf bound_ctrl:1
	s_nop 1
	v_add_u32_dpp v102, v102, v102 row_half_mirror row_mask:0xf bank_mask:0xf bound_ctrl:1
	v_cmp_le_i32_e32 vcc, s6, v102
	v_xor_b32_e32 v103, v98, v100
	s_nop 0
	v_cndmask_b32_e32 v98, v103, v100, vcc
	v_cndmask_b32_e32 v99, v101, v99, vcc
	v_and_b32_e32 v100, v98, v49
	v_or_b32_e32 v101, v99, v100
	v_bcnt_u32_b32 v102, v101, 0
	s_nop 1
	v_add_u32_dpp v102, v102, v102 quad_perm:[1,0,3,2] row_mask:0xf bank_mask:0xf bound_ctrl:1
	s_nop 1
	v_add_u32_dpp v102, v102, v102 quad_perm:[2,3,0,1] row_mask:0xf bank_mask:0xf bound_ctrl:1
	s_nop 1
	v_add_u32_dpp v102, v102, v102 row_half_mirror row_mask:0xf bank_mask:0xf bound_ctrl:1
	v_cmp_le_i32_e32 vcc, s6, v102
	v_xor_b32_e32 v103, v98, v100
	s_nop 0
	v_cndmask_b32_e32 v98, v103, v100, vcc
	v_cndmask_b32_e32 v99, v101, v99, vcc
	v_and_b32_e32 v100, v98, v64
	v_or_b32_e32 v101, v99, v100
	v_bcnt_u32_b32 v102, v101, 0
	s_nop 1
	v_add_u32_dpp v102, v102, v102 quad_perm:[1,0,3,2] row_mask:0xf bank_mask:0xf bound_ctrl:1
	s_nop 1
	v_add_u32_dpp v102, v102, v102 quad_perm:[2,3,0,1] row_mask:0xf bank_mask:0xf bound_ctrl:1
	s_nop 1
	v_add_u32_dpp v102, v102, v102 row_half_mirror row_mask:0xf bank_mask:0xf bound_ctrl:1
	v_cmp_le_i32_e32 vcc, s6, v102
	v_xor_b32_e32 v103, v98, v100
	s_nop 0
	v_cndmask_b32_e32 v98, v103, v100, vcc
	v_cndmask_b32_e32 v99, v101, v99, vcc
	v_and_b32_e32 v100, v98, v63
	v_or_b32_e32 v101, v99, v100
	v_bcnt_u32_b32 v102, v101, 0
	s_nop 1
	v_add_u32_dpp v102, v102, v102 quad_perm:[1,0,3,2] row_mask:0xf bank_mask:0xf bound_ctrl:1
	s_nop 1
	v_add_u32_dpp v102, v102, v102 quad_perm:[2,3,0,1] row_mask:0xf bank_mask:0xf bound_ctrl:1
	s_nop 1
; #define GRP8_SUM(x) do { x += __builtin_amdgcn_update_dpp(0, x, 0xB1, 0xf, 0xf, false); x += __builtin_amdgcn_update_dpp(0, x, 0x4E, 0xf, 0xf, false); x += __builtin_amdgcn_update_dpp(0, x, 0x141, 0xf, 0xf, false); } while (0)
;     ...
;             unsigned Tk = 0u;
; #pragma unroll 1
;     ...
; #pragma unroll
;                 for (int i = 0; i < 32; ++i) cnt += (key[i] >= test) ? 1 : 0;
;                 GRP8_SUM(cnt);
;                 if (cnt >= K) Tk = test; }
	v_add_u32_dpp v102, v102, v102 row_half_mirror row_mask:0xf bank_mask:0xf bound_ctrl:1
	v_cmp_le_i32_e32 vcc, s6, v102
	v_xor_b32_e32 v103, v98, v100
	s_nop 0
	v_cndmask_b32_e32 v98, v103, v100, vcc
	v_cndmask_b32_e32 v99, v101, v99, vcc
	v_and_b32_e32 v100, v98, v62
	v_or_b32_e32 v101, v99, v100
	v_bcnt_u32_b32 v102, v101, 0
	s_nop 1
	v_add_u32_dpp v102, v102, v102 quad_perm:[1,0,3,2] row_mask:0xf bank_mask:0xf bound_ctrl:1
	s_nop 1
	v_add_u32_dpp v102, v102, v102 quad_perm:[2,3,0,1] row_mask:0xf bank_mask:0xf bound_ctrl:1
	s_nop 1
	v_add_u32_dpp v102, v102, v102 row_half_mirror row_mask:0xf bank_mask:0xf bound_ctrl:1
	v_cmp_le_i32_e32 vcc, s6, v102
	v_xor_b32_e32 v103, v98, v100
	s_nop 0
	v_cndmask_b32_e32 v98, v103, v100, vcc
	v_cndmask_b32_e32 v99, v101, v99, vcc
	v_and_b32_e32 v100, v98, v61
	v_or_b32_e32 v101, v99, v100
	v_bcnt_u32_b32 v102, v101, 0
	s_nop 1
	v_add_u32_dpp v102, v102, v102 quad_perm:[1,0,3,2] row_mask:0xf bank_mask:0xf bound_ctrl:1
	s_nop 1
	v_add_u32_dpp v102, v102, v102 quad_perm:[2,3,0,1] row_mask:0xf bank_mask:0xf bound_ctrl:1
	s_nop 1
	v_add_u32_dpp v102, v102, v102 row_half_mirror row_mask:0xf bank_mask:0xf bound_ctrl:1
	v_cmp_le_i32_e32 vcc, s6, v102
	v_xor_b32_e32 v103, v98, v100
	s_nop 0
	v_cndmask_b32_e32 v98, v103, v100, vcc
	v_cndmask_b32_e32 v99, v101, v99, vcc
	v_and_b32_e32 v100, v98, v60
	v_or_b32_e32 v101, v99, v100
	v_bcnt_u32_b32 v102, v101, 0
	s_nop 1
	v_add_u32_dpp v102, v102, v102 quad_perm:[1,0,3,2] row_mask:0xf bank_mask:0xf bound_ctrl:1
	s_nop 1
	v_add_u32_dpp v102, v102, v102 quad_perm:[2,3,0,1] row_mask:0xf bank_mask:0xf bound_ctrl:1
	s_nop 1
	v_add_u32_dpp v102, v102, v102 row_half_mirror row_mask:0xf bank_mask:0xf bound_ctrl:1
	v_cmp_le_i32_e32 vcc, s6, v102
	v_xor_b32_e32 v103, v98, v100
	s_nop 0
	v_cndmask_b32_e32 v98, v103, v100, vcc
	v_cndmask_b32_e32 v99, v101, v99, vcc
	v_and_b32_e32 v100, v98, v59
	v_or_b32_e32 v101, v99, v100
	v_bcnt_u32_b32 v102, v101, 0
	s_nop 1
	v_add_u32_dpp v102, v102, v102 quad_perm:[1,0,3,2] row_mask:0xf bank_mask:0xf bound_ctrl:1
	s_nop 1
	v_add_u32_dpp v102, v102, v102 quad_perm:[2,3,0,1] row_mask:0xf bank_mask:0xf bound_ctrl:1
	s_nop 1
	v_add_u32_dpp v102, v102, v102 row_half_mirror row_mask:0xf bank_mask:0xf bound_ctrl:1
	v_cmp_le_i32_e32 vcc, s6, v102
	v_xor_b32_e32 v103, v98, v100
	s_nop 0
	v_cndmask_b32_e32 v98, v103, v100, vcc
	v_cndmask_b32_e32 v99, v101, v99, vcc
	v_and_b32_e32 v100, v98, v58
	v_or_b32_e32 v101, v99, v100
	v_bcnt_u32_b32 v102, v101, 0
	s_nop 1
	v_add_u32_dpp v102, v102, v102 quad_perm:[1,0,3,2] row_mask:0xf bank_mask:0xf bound_ctrl:1
	s_nop 1
	v_add_u32_dpp v102, v102, v102 quad_perm:[2,3,0,1] row_mask:0xf bank_mask:0xf bound_ctrl:1
	s_nop 1
	v_add_u32_dpp v102, v102, v102 row_half_mirror row_mask:0xf bank_mask:0xf bound_ctrl:1
	v_cmp_le_i32_e32 vcc, s6, v102
	v_xor_b32_e32 v103, v98, v100
	s_nop 0
	v_cndmask_b32_e32 v98, v103, v100, vcc
	v_cndmask_b32_e32 v99, v101, v99, vcc
	v_and_b32_e32 v100, v98, v137
	v_or_b32_e32 v101, v99, v100
	v_bcnt_u32_b32 v102, v101, 0
	s_nop 1
	v_add_u32_dpp v102, v102, v102 quad_perm:[1,0,3,2] row_mask:0xf bank_mask:0xf bound_ctrl:1
	s_nop 1
	v_add_u32_dpp v102, v102, v102 quad_perm:[2,3,0,1] row_mask:0xf bank_mask:0xf bound_ctrl:1
	s_nop 1
	v_add_u32_dpp v102, v102, v102 row_half_mirror row_mask:0xf bank_mask:0xf bound_ctrl:1
	v_cmp_le_i32_e32 vcc, s6, v102
	v_xor_b32_e32 v103, v98, v100
	s_nop 0
	v_cndmask_b32_e32 v98, v103, v100, vcc
	v_cndmask_b32_e32 v99, v101, v99, vcc
	v_and_b32_e32 v100, v98, v48
	v_or_b32_e32 v101, v99, v100
	v_bcnt_u32_b32 v102, v101, 0
	s_nop 1
	v_add_u32_dpp v102, v102, v102 quad_perm:[1,0,3,2] row_mask:0xf bank_mask:0xf bound_ctrl:1
	s_nop 1
	v_add_u32_dpp v102, v102, v102 quad_perm:[2,3,0,1] row_mask:0xf bank_mask:0xf bound_ctrl:1
	s_nop 1
	v_add_u32_dpp v102, v102, v102 row_half_mirror row_mask:0xf bank_mask:0xf bound_ctrl:1
	v_cmp_le_i32_e32 vcc, s6, v102
	v_xor_b32_e32 v103, v98, v100
	s_nop 0
	v_cndmask_b32_e32 v98, v103, v100, vcc
	v_cndmask_b32_e32 v99, v101, v99, vcc
	v_and_b32_e32 v100, v98, v47
	v_or_b32_e32 v101, v99, v100
	v_bcnt_u32_b32 v102, v101, 0
	s_nop 1
	v_add_u32_dpp v102, v102, v102 quad_perm:[1,0,3,2] row_mask:0xf bank_mask:0xf bound_ctrl:1
	s_nop 1
	v_add_u32_dpp v102, v102, v102 quad_perm:[2,3,0,1] row_mask:0xf bank_mask:0xf bound_ctrl:1
	s_nop 1
	v_add_u32_dpp v102, v102, v102 row_half_mirror row_mask:0xf bank_mask:0xf bound_ctrl:1
	v_cmp_le_i32_e32 vcc, s6, v102
	v_xor_b32_e32 v103, v98, v100
	s_nop 0
	v_cndmask_b32_e32 v98, v103, v100, vcc
	v_cndmask_b32_e32 v99, v101, v99, vcc
	v_and_b32_e32 v100, v98, v46
	v_or_b32_e32 v101, v99, v100
	v_bcnt_u32_b32 v102, v101, 0
	s_nop 1
	v_add_u32_dpp v102, v102, v102 quad_perm:[1,0,3,2] row_mask:0xf bank_mask:0xf bound_ctrl:1
	s_nop 1
	v_add_u32_dpp v102, v102, v102 quad_perm:[2,3,0,1] row_mask:0xf bank_mask:0xf bound_ctrl:1
	s_nop 1
	v_add_u32_dpp v102, v102, v102 row_half_mirror row_mask:0xf bank_mask:0xf bound_ctrl:1
; #define GRP8_SUM(x) do { x += __builtin_amdgcn_update_dpp(0, x, 0xB1, 0xf, 0xf, false); x += __builtin_amdgcn_update_dpp(0, x, 0x4E, 0xf, 0xf, false); x += __builtin_amdgcn_update_dpp(0, x, 0x141, 0xf, 0xf, false); } while (0)
;     ...
;             unsigned Tk = 0u;
; #pragma unroll 1
;     ...
; #pragma unroll
;                 for (int i = 0; i < 32; ++i) cnt += (key[i] >= test) ? 1 : 0;
;                 GRP8_SUM(cnt);
;                 if (cnt >= K) Tk = test; }
;             unsigned gt = 0u, eq = 0u;
; #pragma unroll
;             for (int i = 0; i < 32; ++i) { gt |= (key[i] > Tk) ? (1u << i) : 0u; eq |= (key[i] == Tk && Tk != 0u) ? (1u << i) : 0u; }
;             int above = __popc(gt); GRP8_SUM(above);
;             int eqc = __popc(eq), incl = eqc;
;             { int v1 = __builtin_amdgcn_update_dpp(0, incl, 0x111, 0xf, 0xf, false); incl += (sub >= 1) ? v1 : 0;
;               int v2 = __builtin_amdgcn_update_dpp(0, incl, 0x112, 0xf, 0xf, false); incl += (sub >= 2) ? v2 : 0;
;               int v4 = __builtin_amdgcn_update_dpp(0, incl, 0x114, 0xf, 0xf, false); incl += (sub >= 4) ? v4 : 0; }
;             int take = (K - above) - (incl - eqc); take = take < 0 ? 0 : take;
	v_cmp_le_i32_e32 vcc, s6, v102
	v_xor_b32_e32 v103, v98, v100
	s_nop 0
	v_cndmask_b32_e32 v98, v103, v100, vcc
	v_cndmask_b32_e32 v99, v101, v99, vcc
	v_and_b32_e32 v100, v98, v45
	v_or_b32_e32 v101, v99, v100
	v_bcnt_u32_b32 v102, v101, 0
	s_nop 1
	v_add_u32_dpp v102, v102, v102 quad_perm:[1,0,3,2] row_mask:0xf bank_mask:0xf bound_ctrl:1
	s_nop 1
	v_add_u32_dpp v102, v102, v102 quad_perm:[2,3,0,1] row_mask:0xf bank_mask:0xf bound_ctrl:1
	s_nop 1
	v_add_u32_dpp v102, v102, v102 row_half_mirror row_mask:0xf bank_mask:0xf bound_ctrl:1
	v_cmp_le_i32_e32 vcc, s6, v102
	v_xor_b32_e32 v103, v98, v100
	s_nop 0
	v_cndmask_b32_e32 v98, v103, v100, vcc
	v_cndmask_b32_e32 v99, v101, v99, vcc
	v_and_b32_e32 v100, v98, v44
	v_or_b32_e32 v101, v99, v100
	v_bcnt_u32_b32 v102, v101, 0
	s_nop 1
	v_add_u32_dpp v102, v102, v102 quad_perm:[1,0,3,2] row_mask:0xf bank_mask:0xf bound_ctrl:1
	s_nop 1
	v_add_u32_dpp v102, v102, v102 quad_perm:[2,3,0,1] row_mask:0xf bank_mask:0xf bound_ctrl:1
	s_nop 1
	v_add_u32_dpp v102, v102, v102 row_half_mirror row_mask:0xf bank_mask:0xf bound_ctrl:1
	v_cmp_le_i32_e32 vcc, s6, v102
	v_xor_b32_e32 v103, v98, v100
	s_nop 0
	v_cndmask_b32_e32 v98, v103, v100, vcc
	v_cndmask_b32_e32 v99, v101, v99, vcc
	v_and_b32_e32 v100, v98, v43
	v_or_b32_e32 v101, v99, v100
	v_bcnt_u32_b32 v102, v101, 0
	s_nop 1
	v_add_u32_dpp v102, v102, v102 quad_perm:[1,0,3,2] row_mask:0xf bank_mask:0xf bound_ctrl:1
	s_nop 1
	v_add_u32_dpp v102, v102, v102 quad_perm:[2,3,0,1] row_mask:0xf bank_mask:0xf bound_ctrl:1
	s_nop 1
	v_add_u32_dpp v102, v102, v102 row_half_mirror row_mask:0xf bank_mask:0xf bound_ctrl:1
	v_cmp_le_i32_e32 vcc, s6, v102
	v_xor_b32_e32 v103, v98, v100
	s_nop 0
	v_cndmask_b32_e32 v98, v103, v100, vcc
	v_cndmask_b32_e32 v99, v101, v99, vcc
	v_and_b32_e32 v100, v98, v42
	v_or_b32_e32 v101, v99, v100
	v_bcnt_u32_b32 v102, v101, 0
	s_nop 1
	v_add_u32_dpp v102, v102, v102 quad_perm:[1,0,3,2] row_mask:0xf bank_mask:0xf bound_ctrl:1
	s_nop 1
	v_add_u32_dpp v102, v102, v102 quad_perm:[2,3,0,1] row_mask:0xf bank_mask:0xf bound_ctrl:1
	s_nop 1
	v_add_u32_dpp v102, v102, v102 row_half_mirror row_mask:0xf bank_mask:0xf bound_ctrl:1
	v_cmp_le_i32_e32 vcc, s6, v102
	v_xor_b32_e32 v103, v98, v100
	s_nop 0
	v_cndmask_b32_e32 v98, v103, v100, vcc
	v_cndmask_b32_e32 v99, v101, v99, vcc
	v_and_b32_e32 v100, v98, v136
	v_or_b32_e32 v101, v99, v100
	v_bcnt_u32_b32 v102, v101, 0
	s_nop 1
	v_add_u32_dpp v102, v102, v102 quad_perm:[1,0,3,2] row_mask:0xf bank_mask:0xf bound_ctrl:1
	s_nop 1
	v_add_u32_dpp v102, v102, v102 quad_perm:[2,3,0,1] row_mask:0xf bank_mask:0xf bound_ctrl:1
	s_nop 1
	v_add_u32_dpp v102, v102, v102 row_half_mirror row_mask:0xf bank_mask:0xf bound_ctrl:1
	v_cmp_le_i32_e32 vcc, s6, v102
	v_xor_b32_e32 v103, v98, v100
	s_nop 0
	v_cndmask_b32_e32 v98, v103, v100, vcc
	v_cndmask_b32_e32 v99, v101, v99, vcc
	v_mov_b32_e32 v42, v99
	v_and_b32_e32 v44, v98, v115
	v_mov_b32_e32 v75, 0x80
	v_mov_b32_e32 v76, 0x100
	v_mov_b32_e32 v77, 0x200
	v_mov_b32_e32 v78, 0x400
	v_mov_b32_e32 v79, 0x800
	v_mov_b32_e32 v80, 0x1000
	v_mov_b32_e32 v81, 0x2000
	v_mov_b32_e32 v82, 0x4000
	v_mov_b32_e32 v83, 0x8000
	v_mov_b32_e32 v84, 0x10000
	v_mov_b32_e32 v85, 0x20000
	v_mov_b32_e32 v86, 0x40000
	v_mov_b32_e32 v87, 0x80000
	v_mov_b32_e32 v88, 0x100000
	v_mov_b32_e32 v89, 0x200000
	v_mov_b32_e32 v90, 0x400000
	v_mov_b32_e32 v91, 0x800000
	v_mov_b32_e32 v92, 0x1000000
	v_mov_b32_e32 v93, 0x2000000
	v_mov_b32_e32 v94, 0x4000000
	v_mov_b32_e32 v95, 0x8000000
	v_mov_b32_e32 v96, 0x10000000
	v_mov_b32_e32 v97, 0x20000000
	v_readlane_b32 s8, v254, 37
	v_bcnt_u32_b32 v43, v42, 0
	v_mov_b32_e32 v45, v1
	v_mov_b32_e32 v46, v1
	v_readlane_b32 s9, v254, 38
	v_mov_b32_dpp v45, v43 quad_perm:[1,0,3,2] row_mask:0xf bank_mask:0xf
	v_bcnt_u32_b32 v43, v42, v45
	v_bcnt_u32_b32 v45, v44, 0
	v_bcnt_u32_b32 v47, v44, s6
	v_add_u32_dpp v43, v43, v43 quad_perm:[2,3,0,1] row_mask:0xf bank_mask:0xf bound_ctrl:1
	v_mov_b32_dpp v46, v45 row_shr:1 row_mask:0xf bank_mask:0xf
	v_cndmask_b32_e64 v45, v46, 0, s[8:9]
	v_bcnt_u32_b32 v45, v44, v45
	v_mov_b32_e32 v46, v1
	v_readlane_b32 s8, v254, 39
	v_readlane_b32 s9, v254, 40
	v_mov_b32_dpp v46, v45 row_shr:2 row_mask:0xf bank_mask:0xf
	v_add_u32_dpp v43, v43, v43 row_half_mirror row_mask:0xf bank_mask:0xf bound_ctrl:1
	v_cndmask_b32_e64 v46, 0, v46, s[8:9]
	v_add_u32_e32 v45, v45, v46
	v_mov_b32_e32 v46, v1
	v_readlane_b32 s8, v254, 41
	v_readlane_b32 s9, v254, 42
	v_mov_b32_dpp v46, v45 row_shr:4 row_mask:0xf bank_mask:0xf
	v_bfrev_b32_e32 v73, 1
	v_cndmask_b32_e64 v46, 0, v46, s[8:9]
	v_add3_u32 v43, v43, v46, v45
	v_sub_u32_e32 v45, v47, v43
	v_cmp_lt_i32_e32 vcc, 0, v45
	v_cmp_ne_u32_e64 s[14:15], 0, v44
	v_mov_b32_e32 v43, 0
	s_and_b64 s[8:9], s[14:15], vcc
	s_mov_b64 s[6:7], exec
	s_and_b64 s[8:9], s[6:7], s[8:9]
	v_mov_b32_e32 v234, 0x358637bd
	s_mov_b64 exec, s[8:9]
	s_cbranch_execz .LBB0_855
	v_mov_b32_e32 v43, 0
	s_mov_b64 s[8:9], 0
